# speedup vs baseline: 1.0667x; 1.0667x over previous
.LBB0_60:
	s_andn2_b64 vcc, exec, s[4:5]
	s_cbranch_vccnz .LBB0_98
	s_cmpk_gt_u32 s2, 122
	s_cbranch_scc1 .LBB0_98
	s_load_dwordx2 s[4:5], s[0:1], 0x0
	s_load_dwordx4 s[12:15], s[0:1], 0x30
	s_lshl_b32 s3, s2, 13
	v_lshlrev_b32_e32 v1, 2, v0
	v_mov_b32_e32 v2, 0
	ds_write_b32 v1, v2
	v_or_b32_e32 v3, s3, v0
	s_mov_b32 s10, 0xf423f
	s_waitcnt lgkmcnt(0)
	s_add_u32 s6, s4, 0x3d0900
	s_addc_u32 s7, s5, 0
	v_min_u32_e32 v4, s10, v3
	v_lshlrev_b32_e32 v4, 2, v4
	global_load_dword v16, v4, s[6:7] nt
	global_load_dword v32, v4, s[4:5] nt
	v_add_u32_e32 v5, 1024, v3
	v_min_u32_e32 v5, s10, v5
	v_lshlrev_b32_e32 v5, 2, v5
	global_load_dword v17, v5, s[6:7] nt
	global_load_dword v33, v5, s[4:5] nt
	v_add_u32_e32 v6, 2048, v3
	v_min_u32_e32 v6, s10, v6
	v_lshlrev_b32_e32 v6, 2, v6
	global_load_dword v18, v6, s[6:7] nt
	global_load_dword v34, v6, s[4:5] nt
	v_add_u32_e32 v7, 3072, v3
	v_min_u32_e32 v7, s10, v7
	v_lshlrev_b32_e32 v7, 2, v7
	global_load_dword v19, v7, s[6:7] nt
	global_load_dword v35, v7, s[4:5] nt
	v_add_u32_e32 v4, 4096, v3
	v_min_u32_e32 v4, s10, v4
	v_lshlrev_b32_e32 v4, 2, v4
	global_load_dword v20, v4, s[6:7] nt
	global_load_dword v36, v4, s[4:5] nt
	v_add_u32_e32 v5, 5120, v3
	v_min_u32_e32 v5, s10, v5
	v_lshlrev_b32_e32 v5, 2, v5
	global_load_dword v21, v5, s[6:7] nt
	global_load_dword v37, v5, s[4:5] nt
	v_add_u32_e32 v6, 6144, v3
	v_min_u32_e32 v6, s10, v6
	v_lshlrev_b32_e32 v6, 2, v6
	global_load_dword v22, v6, s[6:7] nt
	global_load_dword v38, v6, s[4:5] nt
	v_add_u32_e32 v7, 7168, v3
	v_min_u32_e32 v7, s10, v7
	v_lshlrev_b32_e32 v7, 2, v7
	global_load_dword v23, v7, s[6:7] nt
	global_load_dword v39, v7, s[4:5] nt
	s_barrier
	s_mov_b32 s11, 0x5397829d
	s_mov_b32 s10, 0xf4240
	v_mov_b32_e32 v8, 0xffc
	s_waitcnt vmcnt(0)
	v_cmp_gt_u32_e32 vcc, s10, v3
	v_mul_hi_u32 v4, v16, s11
	v_lshrrev_b32_e32 v4, 5, v4
	v_mul_u32_u24_e32 v5, 0x62, v4
	v_sub_u32_e32 v5, v16, v5
	v_lshl_or_b32 v32, v5, 17, v32
	v_lshlrev_b32_e32 v4, 2, v4
	v_cndmask_b32_e32 v16, v8, v4, vcc
	v_add_u32_e32 v6, 1024, v3
	v_cmp_gt_u32_e32 vcc, s10, v6
	v_mul_hi_u32 v4, v17, s11
	v_lshrrev_b32_e32 v4, 5, v4
	v_mul_u32_u24_e32 v5, 0x62, v4
	v_sub_u32_e32 v5, v17, v5
	v_lshl_or_b32 v33, v5, 17, v33
	v_lshlrev_b32_e32 v4, 2, v4
	v_cndmask_b32_e32 v17, v8, v4, vcc
	v_add_u32_e32 v6, 2048, v3
	v_cmp_gt_u32_e32 vcc, s10, v6
	v_mul_hi_u32 v4, v18, s11
	v_lshrrev_b32_e32 v4, 5, v4
	v_mul_u32_u24_e32 v5, 0x62, v4
	v_sub_u32_e32 v5, v18, v5
	v_lshl_or_b32 v34, v5, 17, v34
	v_lshlrev_b32_e32 v4, 2, v4
	v_cndmask_b32_e32 v18, v8, v4, vcc
	v_add_u32_e32 v6, 3072, v3
	v_cmp_gt_u32_e32 vcc, s10, v6
	v_mul_hi_u32 v4, v19, s11
	v_lshrrev_b32_e32 v4, 5, v4
	v_mul_u32_u24_e32 v5, 0x62, v4
	v_sub_u32_e32 v5, v19, v5
	v_lshl_or_b32 v35, v5, 17, v35
	v_lshlrev_b32_e32 v4, 2, v4
	v_cndmask_b32_e32 v19, v8, v4, vcc
	v_add_u32_e32 v6, 4096, v3
	v_cmp_gt_u32_e32 vcc, s10, v6
	v_mul_hi_u32 v4, v20, s11
	v_lshrrev_b32_e32 v4, 5, v4
	v_mul_u32_u24_e32 v5, 0x62, v4
	v_sub_u32_e32 v5, v20, v5
	v_lshl_or_b32 v36, v5, 17, v36
	v_lshlrev_b32_e32 v4, 2, v4
	v_cndmask_b32_e32 v20, v8, v4, vcc
	v_add_u32_e32 v6, 5120, v3
	v_cmp_gt_u32_e32 vcc, s10, v6
	v_mul_hi_u32 v4, v21, s11
	v_lshrrev_b32_e32 v4, 5, v4
	v_mul_u32_u24_e32 v5, 0x62, v4
	v_sub_u32_e32 v5, v21, v5
	v_lshl_or_b32 v37, v5, 17, v37
	v_lshlrev_b32_e32 v4, 2, v4
	v_cndmask_b32_e32 v21, v8, v4, vcc
	v_add_u32_e32 v6, 6144, v3
	v_cmp_gt_u32_e32 vcc, s10, v6
	v_mul_hi_u32 v4, v22, s11
	v_lshrrev_b32_e32 v4, 5, v4
	v_mul_u32_u24_e32 v5, 0x62, v4
	v_sub_u32_e32 v5, v22, v5
	v_lshl_or_b32 v38, v5, 17, v38
	v_lshlrev_b32_e32 v4, 2, v4
	v_cndmask_b32_e32 v22, v8, v4, vcc
	v_add_u32_e32 v6, 7168, v3
	v_cmp_gt_u32_e32 vcc, s10, v6
	v_mul_hi_u32 v4, v23, s11
	v_lshrrev_b32_e32 v4, 5, v4
	v_mul_u32_u24_e32 v5, 0x62, v4
	v_sub_u32_e32 v5, v23, v5
	v_lshl_or_b32 v39, v5, 17, v39
	v_lshlrev_b32_e32 v4, 2, v4
	v_cndmask_b32_e32 v23, v8, v4, vcc
	v_mov_b32_e32 v7, 1
	ds_add_rtn_u32 v48, v16, v7
	ds_add_rtn_u32 v49, v17, v7
	ds_add_rtn_u32 v50, v18, v7
	ds_add_rtn_u32 v51, v19, v7
	ds_add_rtn_u32 v52, v20, v7
	ds_add_rtn_u32 v53, v21, v7
	ds_add_rtn_u32 v54, v22, v7
	ds_add_rtn_u32 v55, v23, v7
	s_waitcnt lgkmcnt(0)
	s_barrier
	ds_read_b32 v4, v1
	v_and_b32_e32 v8, 63, v0
	v_lshrrev_b32_e32 v9, 6, v0
	s_waitcnt lgkmcnt(0)
	v_add_u32_dpp v5, v4, v4 row_shr:1 row_mask:0xf bank_mask:0xf bound_ctrl:1
	s_nop 1
	v_add_u32_dpp v5, v5, v5 row_shr:2 row_mask:0xf bank_mask:0xf bound_ctrl:1
	s_nop 1
	v_add_u32_dpp v5, v5, v5 row_shr:4 row_mask:0xf bank_mask:0xf bound_ctrl:1
	s_nop 1
	v_add_u32_dpp v5, v5, v5 row_shr:8 row_mask:0xf bank_mask:0xf bound_ctrl:1
	s_nop 1
	v_add_u32_dpp v5, v5, v5 row_bcast:15 row_mask:0xa bank_mask:0xf
	s_nop 1
	v_add_u32_dpp v5, v5, v5 row_bcast:31 row_mask:0xc bank_mask:0xf
	v_readfirstlane_b32 s9, v9
	s_nop 0
	v_readlane_b32 s8, v5, 63
	s_lshl_b32 s16, s9, 2
	v_mov_b32_e32 v10, s16
	s_nop 1
	v_mov_b32_e32 v11, s8
	ds_write_b32 v10, v11 offset:4096
	s_waitcnt lgkmcnt(0)
	s_barrier
	v_min_u32_e32 v10, 15, v8
	v_lshlrev_b32_e32 v10, 2, v10
	ds_read_b32 v11, v10 offset:4096
	v_cmp_gt_u32_e32 vcc, s9, v8
	v_sub_u32_e32 v5, v5, v4
	s_waitcnt lgkmcnt(0)
	v_cndmask_b32_e32 v11, 0, v11, vcc
	s_nop 1
	v_add_u32_dpp v11, v11, v11 row_shr:1 row_mask:0xf bank_mask:0xf bound_ctrl:1
	s_nop 1
	v_add_u32_dpp v11, v11, v11 row_shr:2 row_mask:0xf bank_mask:0xf bound_ctrl:1
	s_nop 1
	v_add_u32_dpp v11, v11, v11 row_shr:4 row_mask:0xf bank_mask:0xf bound_ctrl:1
	s_nop 1
	v_add_u32_dpp v11, v11, v11 row_shr:8 row_mask:0xf bank_mask:0xf bound_ctrl:1
	s_nop 1
	v_readlane_b32 s17, v11, 15
	s_nop 3
	v_add_u32_e32 v5, s17, v5
	ds_write_b32 v1, v5
	s_waitcnt lgkmcnt(0)
	s_barrier
	s_mulk_i32 s2, 0x3fe
	v_add_u32_e32 v10, s2, v0
	v_lshlrev_b32_e32 v10, 2, v10
	s_movk_i32 s16, 0x3fe
	v_cmp_gt_u32_e32 vcc, s16, v0
	s_and_saveexec_b64 s[8:9], vcc
	s_cbranch_execz .Lk1p_o
	global_store_dword v10, v5, s[14:15] sc1
.Lk1p_o:
	s_mov_b64 exec, s[8:9]
	ds_read_b32 v16, v16
	ds_read_b32 v17, v17
	ds_read_b32 v18, v18
	ds_read_b32 v19, v19
	ds_read_b32 v20, v20
	ds_read_b32 v21, v21
	ds_read_b32 v22, v22
	ds_read_b32 v23, v23
	s_waitcnt lgkmcnt(0)
	v_add_u32_e32 v4, v16, v48
	v_lshlrev_b32_e32 v4, 2, v4
	ds_write_b32 v4, v32 offset:4352
	v_add_u32_e32 v5, v17, v49
	v_lshlrev_b32_e32 v5, 2, v5
	ds_write_b32 v5, v33 offset:4352
	v_add_u32_e32 v6, v18, v50
	v_lshlrev_b32_e32 v6, 2, v6
	ds_write_b32 v6, v34 offset:4352
	v_add_u32_e32 v7, v19, v51
	v_lshlrev_b32_e32 v7, 2, v7
	ds_write_b32 v7, v35 offset:4352
	v_add_u32_e32 v4, v20, v52
	v_lshlrev_b32_e32 v4, 2, v4
	ds_write_b32 v4, v36 offset:4352
	v_add_u32_e32 v5, v21, v53
	v_lshlrev_b32_e32 v5, 2, v5
	ds_write_b32 v5, v37 offset:4352
	v_add_u32_e32 v6, v22, v54
	v_lshlrev_b32_e32 v6, 2, v6
	ds_write_b32 v6, v38 offset:4352
	v_add_u32_e32 v7, v23, v55
	v_lshlrev_b32_e32 v7, 2, v7
	ds_write_b32 v7, v39 offset:4352
	s_waitcnt lgkmcnt(0)
	s_barrier
	s_sub_u32 s16, 0xf4240, s3
	s_min_u32 s16, s16, 0x2000
	v_lshlrev_b32_e32 v4, 3, v0
	v_cmp_gt_u32_e32 vcc, s16, v4
	s_and_saveexec_b64 s[8:9], vcc
	s_cbranch_execz .LBB0_98
	v_lshlrev_b32_e32 v5, 5, v0
	ds_read_b128 v[16:19], v5 offset:4352
	ds_read_b128 v[20:23], v5 offset:4368
	s_lshl_b32 s16, s3, 2
	v_add_u32_e32 v6, s16, v5
	s_waitcnt lgkmcnt(0)
	global_store_dwordx4 v6, v[16:19], s[12:13] sc1
	global_store_dwordx4 v6, v[20:23], s[12:13] offset:16 sc1

	.amdhsa_kernel _Z6k_partPKiPKfS2_S2_S2_S2_PiS3_PDF16_S4_S4_
		.amdhsa_group_segment_fixed_size 37120
		.amdhsa_private_segment_fixed_size 0
		.amdhsa_kernarg_size 88
		.amdhsa_user_sgpr_count 2
		.amdhsa_user_sgpr_dispatch_ptr 0
		.amdhsa_user_sgpr_queue_ptr 0
		.amdhsa_user_sgpr_kernarg_segment_ptr 1
		.amdhsa_user_sgpr_dispatch_id 0
		.amdhsa_user_sgpr_kernarg_preload_length 0
		.amdhsa_user_sgpr_kernarg_preload_offset 0
		.amdhsa_user_sgpr_private_segment_size 0
		.amdhsa_uses_dynamic_stack 0
		.amdhsa_enable_private_segment 0
		.amdhsa_system_sgpr_workgroup_id_x 1
		.amdhsa_system_sgpr_workgroup_id_y 0
		.amdhsa_system_sgpr_workgroup_id_z 0
		.amdhsa_system_sgpr_workgroup_info 0
		.amdhsa_system_vgpr_workitem_id 0
		.amdhsa_next_free_vgpr 64
		.amdhsa_next_free_sgpr 22
		.amdhsa_accum_offset 64
		.amdhsa_reserve_vcc 1
		.amdhsa_float_round_mode_32 0
		.amdhsa_float_round_mode_16_64 0
		.amdhsa_float_denorm_mode_32 3
		.amdhsa_float_denorm_mode_16_64 3
		.amdhsa_dx10_clamp 1
		.amdhsa_ieee_mode 1
		.amdhsa_fp16_overflow 0
		.amdhsa_tg_split 0
		.amdhsa_exception_fp_ieee_invalid_op 0
		.amdhsa_exception_fp_denorm_src 0
		.amdhsa_exception_fp_ieee_div_zero 0
		.amdhsa_exception_fp_ieee_overflow 0
		.amdhsa_exception_fp_ieee_underflow 0
		.amdhsa_exception_fp_ieee_inexact 0
		.amdhsa_exception_int_div_zero 0
	.end_amdhsa_kernel

.Lk2f_l2:
	v_mov_b32_e32 v8, 0
	v_mov_b32_e32 v9, 0
	s_cmp_lt_u32 s4, 4
	s_cbranch_scc0 .Lk2f_l3
	s_movk_i32 s5, 0xf6
	v_cmp_gt_u32_e32 vcc, s5, v0
	v_mov_b32_e32 v23, s3
	s_movk_i32 s5, 0x3fe
	v_lshrrev_b32_e32 v22, 1, v0
	v_mad_u32_u24 v23, v22, s5, v23
	v_lshlrev_b32_e32 v23, 2, v23
	s_and_saveexec_b64 s[6:7], vcc
	global_load_dwordx2 v[8:9], v23, s[12:13]
	s_mov_b64 exec, s[6:7]
.Lk2f_l3:
	s_waitcnt vmcnt(0)
	s_cmp_lt_u32 s4, 4
	s_cbranch_scc0 .Lk2f_l4
	v_and_b32_e32 v42, 1, v0
	v_lshrrev_b32_e32 v25, 1, v0
	v_lshl_add_u32 v43, v42, 4, v8
	v_min_u32_e32 v25, 122, v25
	v_sub_u32_e32 v24, v9, v43
	v_lshlrev_b32_e32 v25, 15, v25
	v_max_i32_e32 v24, 0, v24
	v_cmp_ne_u32_e32 vcc, 1, v42
	v_min_i32_e32 v44, 16, v24
	v_lshl_add_u32 v25, v43, 2, v25
	v_cndmask_b32_e32 v24, v24, v44, vcc
	v_cmp_eq_u32_e32 vcc, 0, v42
	v_cmp_lt_i32_e64 s[38:39], 0, v24
	v_cmp_lt_i32_e64 s[40:41], 4, v24
	v_cmp_lt_i32_e64 s[42:43], 8, v24
	v_cmp_lt_i32_e64 s[44:45], 12, v24
	v_cndmask_b32_e32 v8, 0, v8, vcc
	s_mov_b64 exec, s[38:39]
	s_cbranch_execz .Lk2f_p0
	global_load_dwordx4 v[26:29], v25, s[10:11]
.Lk2f_p0:
	s_mov_b64 exec, s[40:41]
	s_cbranch_execz .Lk2f_p1
	global_load_dwordx4 v[30:33], v25, s[10:11] offset:16
.Lk2f_p1:
	s_mov_b64 exec, s[42:43]
	s_cbranch_execz .Lk2f_p2
	global_load_dwordx4 v[34:37], v25, s[10:11] offset:32
.Lk2f_p2:
	s_mov_b64 exec, s[44:45]
	s_cbranch_execz .Lk2f_p3
	global_load_dwordx4 v[38:41], v25, s[10:11] offset:48
.Lk2f_p3:
	s_mov_b64 exec, -1
	v_add_u32_dpp v42, v8, v8 row_shr:1 row_mask:0xf bank_mask:0xf bound_ctrl:1
	s_nop 1
	v_add_u32_dpp v42, v42, v42 row_shr:2 row_mask:0xf bank_mask:0xf bound_ctrl:1
	s_nop 1
	v_add_u32_dpp v42, v42, v42 row_shr:4 row_mask:0xf bank_mask:0xf bound_ctrl:1
	s_nop 1
	v_add_u32_dpp v42, v42, v42 row_shr:8 row_mask:0xf bank_mask:0xf bound_ctrl:1
	s_nop 1
	v_add_u32_dpp v42, v42, v42 row_bcast:15 row_mask:0xa bank_mask:0xf
	s_nop 1
	v_add_u32_dpp v42, v42, v42 row_bcast:31 row_mask:0xc bank_mask:0xf
	s_lshl_b32 s5, s4, 2
	v_mov_b32_e32 v43, s5
	v_readlane_b32 s5, v42, 63
	s_nop 3
	v_mov_b32_e32 v42, s5
	ds_write_b32 v43, v42 offset:19216

amdhsa.kernels:
  - .agpr_count:     0
    .args:
      - .actual_access:  read_only
        .address_space:  global
        .offset:         0
        .size:           8
        .value_kind:     global_buffer
      - .actual_access:  read_only
        .address_space:  global
        .offset:         8
        .size:           8
        .value_kind:     global_buffer
      - .actual_access:  read_only
        .address_space:  global
        .offset:         16
        .size:           8
        .value_kind:     global_buffer
      - .actual_access:  read_only
        .address_space:  global
        .offset:         24
        .size:           8
        .value_kind:     global_buffer
      - .actual_access:  read_only
        .address_space:  global
        .offset:         32
        .size:           8
        .value_kind:     global_buffer
      - .actual_access:  read_only
        .address_space:  global
        .offset:         40
        .size:           8
        .value_kind:     global_buffer
      - .actual_access:  write_only
        .address_space:  global
        .offset:         48
        .size:           8
        .value_kind:     global_buffer
      - .actual_access:  write_only
        .address_space:  global
        .offset:         56
        .size:           8
        .value_kind:     global_buffer
      - .actual_access:  write_only
        .address_space:  global
        .offset:         64
        .size:           8
        .value_kind:     global_buffer
      - .actual_access:  write_only
        .address_space:  global
        .offset:         72
        .size:           8
        .value_kind:     global_buffer
      - .actual_access:  write_only
        .address_space:  global
        .offset:         80
        .size:           8
        .value_kind:     global_buffer
    .group_segment_fixed_size: 37120
    .kernarg_segment_align: 8
    .kernarg_segment_size: 88
    .language:       OpenCL C
    .language_version:
      - 2
      - 0
    .max_flat_workgroup_size: 1024
    .name:           _Z6k_partPKiPKfS2_S2_S2_S2_PiS3_PDF16_S4_S4_
    .private_segment_fixed_size: 0
    .sgpr_count:     28
    .sgpr_spill_count: 0
    .symbol:         _Z6k_partPKiPKfS2_S2_S2_S2_PiS3_PDF16_S4_S4_.kd
    .uniform_work_group_size: 1
    .uses_dynamic_stack: false
    .vgpr_count:     64
    .vgpr_spill_count: 0
    .wavefront_size: 64
  - .agpr_count:     0
    .args:
      - .actual_access:  read_only
        .address_space:  global
        .offset:         0
        .size:           8
        .value_kind:     global_buffer
      - .actual_access:  read_only
        .address_space:  global
        .offset:         8
        .size:           8
        .value_kind:     global_buffer
      - .actual_access:  read_only
        .address_space:  global
        .offset:         16
        .size:           8
        .value_kind:     global_buffer
      - .actual_access:  write_only
        .address_space:  global
        .offset:         24
        .size:           8
        .value_kind:     global_buffer
      - .address_space:  global
        .offset:         32
        .size:           8
        .value_kind:     global_buffer
      - .actual_access:  read_only
        .address_space:  global
        .offset:         40
        .size:           8
        .value_kind:     global_buffer
      - .actual_access:  read_only
        .address_space:  global
        .offset:         48
        .size:           8
        .value_kind:     global_buffer
      - .actual_access:  read_only
        .address_space:  global
        .offset:         56
        .size:           8
        .value_kind:     global_buffer
      - .actual_access:  read_only
        .address_space:  global
        .offset:         64
        .size:           8
        .value_kind:     global_buffer
      - .actual_access:  write_only
        .address_space:  global
        .offset:         72
        .size:           8
        .value_kind:     global_buffer
      - .actual_access:  write_only
        .address_space:  global
        .offset:         80
        .size:           8
        .value_kind:     global_buffer
    .group_segment_fixed_size: 33712
    .kernarg_segment_align: 8
    .kernarg_segment_size: 88
    .language:       OpenCL C
    .language_version:
      - 2
      - 0
    .max_flat_workgroup_size: 512
    .name:           _Z8k_layer1PKDF16_PKiS2_PiS3_PKDv4_jS6_PKfS8_P15HIP_vector_typeIfLj2EESB_
    .private_segment_fixed_size: 0
    .sgpr_count:     76
    .sgpr_spill_count: 0
    .symbol:         _Z8k_layer1PKDF16_PKiS2_PiS3_PKDv4_jS6_PKfS8_P15HIP_vector_typeIfLj2EESB_.kd
    .uniform_work_group_size: 1
    .uses_dynamic_stack: false
    .vgpr_count:     64
    .vgpr_spill_count: 0
    .wavefront_size: 64
  - .agpr_count:     0
    .args:
      - .actual_access:  read_only
        .address_space:  global
        .offset:         0
        .size:           8
        .value_kind:     global_buffer
      - .actual_access:  read_only
        .address_space:  global
        .offset:         8
        .size:           8
        .value_kind:     global_buffer
      - .actual_access:  read_only
        .address_space:  global
        .offset:         16
        .size:           8
        .value_kind:     global_buffer
      - .actual_access:  read_only
        .address_space:  global
        .offset:         24
        .size:           8
        .value_kind:     global_buffer
      - .actual_access:  write_only
        .address_space:  global
        .offset:         32
        .size:           8
        .value_kind:     global_buffer
    .group_segment_fixed_size: 0
    .kernarg_segment_align: 8
    .kernarg_segment_size: 40
    .language:       OpenCL C
    .language_version:
      - 2
      - 0
    .max_flat_workgroup_size: 448
    .name:           _Z8k_layer2PK15HIP_vector_typeIfLj2EES2_PKiS4_PS0_
    .private_segment_fixed_size: 0
    .sgpr_count:     21
    .sgpr_spill_count: 0
    .symbol:         _Z8k_layer2PK15HIP_vector_typeIfLj2EES2_PKiS4_PS0_.kd
    .uniform_work_group_size: 1
    .uses_dynamic_stack: false
    .vgpr_count:     25
    .vgpr_spill_count: 0
    .wavefront_size: 64
